# attention: half-step stagger of odd vs even waves (extra mid-step barrier) so the two waves of a SIMD alternate MFMA and softmax VALU work
# speedup vs baseline: 1.0035x; 1.0035x over previous
; __device__ __forceinline__ void phase_attention(const Frame& F, const Args& a) {
;     constexpr int ABUF = 35840;
;     const bf16_t* QK = (const bf16_t*)(F.ws + WS_Z); const bf16_t* VT = (const bf16_t*)(F.ws + WS_YTL); bf16_t* O = (bf16_t*)(F.ws + WS_MIX);
;     const int fr = F.lane & 15, fq = F.lane >> 4;
;     const int key0 = F.tid >> 4, c16 = F.tid & 15, dim0 = F.tid >> 3, c8 = F.tid & 7;
;     for (int unit = ((F.G % 8 == 0) ? (F.bid % 8) * (F.G / 8) + F.bid / 8 : F.bid); unit < 256; unit += F.G) {
;         const int b = unit >> 7, h = (unit >> 5) & 3, n = unit & 31;
;         const int kt_lo = (2 * n - 2) < 0 ? 0 : (2 * n - 2), kt_hi = (2 * n + 3) > 63 ? 63 : (2 * n + 3), nband = kt_hi - kt_lo + 1, ntile = nband + 4, nstep = 2 * ntile;
;         u32x4 kreg[2], vreg[2];
;         const bf16_t* kbase = QK + 2048 + h * 128 + 8 * c16; const bf16_t* vbase = VT + (size_t)(h * 128 + dim0) * T0 + 8 * c8;
;     ...
;         __syncthreads();
;         ATT_LOAD(0); ATT_STORE(0);
;         __syncthreads();
;         bf16x8 aq[2][4]; float mrun[2], lrun[2]; f32x4 o[2][8]; int qh = 0, qpos0 = 0, qrow = 0;
.LBB0_2767:
	s_cmp_lt_i32 s94, 14
	s_cselect_b64 s[0:1], -1, 0
	s_and_b64 s[4:5], s[0:1], s[4:5]
	s_andn2_b64 vcc, exec, s[4:5]
	s_cbranch_vccnz .LBB0_2792
	v_readlane_b32 s0, v254, 0
	v_readlane_b32 s1, v254, 1
	s_mov_b32 s2, s0
	s_ashr_i32 s1, s2, 3
	s_ashr_i32 s2, s3, 31
	s_lshr_b32 s2, s2, 29
	s_add_i32 s2, s3, s2
	s_and_b32 s6, s2, -8
	s_sub_i32 s6, s3, s6
	s_mul_i32 s1, s1, s6
	s_ashr_i32 s2, s2, 3
	s_and_b32 s0, s0, 7
	s_add_i32 s1, s1, s2
	s_cmp_eq_u32 s0, 0
	s_cselect_b32 s18, s1, s3
	s_cmpk_gt_i32 s18, 0xff
	s_mov_b32 s7, 0
	s_cbranch_scc1 .LBB0_2792
	v_lshlrev_b32_e32 v6, 3, v0
	v_and_b32_e32 v2, 0x78, v6
	v_lshlrev_b32_e32 v150, 1, v2
	v_mov_b32_e32 v2, 0
	v_mov_b32_e32 v151, v2
	v_lshl_add_u64 v[4:5], s[92:93], 0, v[150:151]
	s_mov_b64 s[0:1], 0x3a601000
	v_lshl_add_u64 v[152:153], v[4:5], 0, s[0:1]
	v_and_b32_e32 v4, 56, v6
	v_lshlrev_b32_e32 v154, 1, v4
	v_mov_b32_e32 v155, v2
	v_lshl_add_u64 v[4:5], s[92:93], 0, v[154:155]
	s_mov_b64 s[0:1], 0x3d900000
	v_lshl_add_u64 v[156:157], v[4:5], 0, s[0:1]
	v_and_b32_e32 v4, 48, v1
	v_mov_b32_e32 v5, v2
	v_lshrrev_b32_e32 v3, 4, v1
	v_lshl_add_u64 v[4:5], s[92:93], 0, v[4:5]
	s_mov_b64 s[0:1], 0x3a600000
	v_lshl_add_u64 v[158:159], v[4:5], 0, s[0:1]
	v_lshlrev_b32_e32 v4, 2, v3
	v_mov_b32_e32 v5, v2
	v_and_b32_e32 v172, 15, v0
	v_lshrrev_b32_e32 v173, 4, v0
	v_lshrrev_b32_e32 v174, 3, v0
	v_lshl_add_u64 v[6:7], s[92:93], 0, v[4:5]
	s_mov_b64 s[0:1], 0x41b00000
	v_mul_u32_u24_e32 v8, 0x88, v173
	v_mul_u32_u24_e32 v9, 0x48, v174
	v_lshlrev_b32_e32 v151, 3, v3
	v_lshl_add_u64 v[160:161], v[6:7], 0, s[0:1]
	v_sub_u32_e32 v3, v4, v172
	v_readlane_b32 s0, v254, 2
	v_lshlrev_b32_e32 v177, 1, v8
	v_lshlrev_b32_e32 v179, 1, v9
	v_add_u32_e32 v181, 0xffffff7f, v3
	s_lshr_b32 s19, s0, 8
	s_lshl_b32 s0, s74, 5
	v_mbcnt_lo_u32_b32 v3, -1, 0
	v_and_b32_e32 v155, 48, v0
	v_mul_u32_u24_e32 v175, 0x110, v172
	v_mul_u32_u24_e32 v176, 0x90, v172
	v_add3_u32 v178, 0, v177, v150
	v_add3_u32 v180, 0, v179, v154
	v_readfirstlane_b32 s98, v0
	s_bfe_u32 s98, s98, 0x10006
	s_and_b32 s20, s0, 0x60
	s_movk_i32 s21, 0x1400
	s_mov_b64 s[8:9], 0x110000
	s_movk_i32 s22, 0xfeff
	s_mov_b32 s23, 0xff800000
	s_movk_i32 s24, 0xfefe
	s_mov_b32 s25, 0x41800000
	s_mov_b32 s26, 0xc3e00000
	v_mbcnt_hi_u32_b32 v182, -1, v3
	v_mov_b32_e32 v183, 0xff800000
	v_mov_b32_e32 v184, 0x43e00000
	s_branch .LBB0_2772
.LBB0_2770:
	s_cmp_lg_u32 s98, 0
	s_cbranch_scc1 .Latt_trail0
	s_barrier

; __device__ __forceinline__ void phase_attention(const Frame& F, const Args& a) {
;     ...
;         u32x4 kreg[2], vreg[2];
;         const bf16_t* kbase = QK + 2048 + h * 128 + 8 * c16; const bf16_t* vbase = VT + (size_t)(h * 128 + dim0) * T0 + 8 * c8;
;     ...
;         __syncthreads();
;         ATT_LOAD(0); ATT_STORE(0);
;         __syncthreads();
;         bf16x8 aq[2][4]; float mrun[2], lrun[2]; f32x4 o[2][8]; int qh = 0, qpos0 = 0, qrow = 0;
;         for (int step = 0; step < nstep; ++step) {
.LBB0_2776:
	s_bfe_u32 s10, s18, 0x20005
	s_lshl_b32 s1, s10, 7
	v_or_b32_e32 v3, s1, v174
	v_mul_u32_u24_e32 v66, 0x4400, v3
	s_lshl_b32 s6, s1, 1
	v_mov_b32_e32 v67, v2
	v_lshl_add_u64 v[162:163], v[152:153], 0, s[6:7]
	v_lshl_add_u64 v[164:165], v[156:157], 0, v[66:67]
	v_add_u32_e32 v3, s0, v173
	s_ashr_i32 s1, s0, 31
	v_mad_i64_i32 v[66:67], s[16:17], v3, s21, v[162:163]
	v_add_u32_e32 v3, 32, v3
	s_lshl_b64 s[0:1], s[0:1], 1
	v_lshl_add_u64 v[166:167], v[164:165], 0, s[8:9]
	v_mad_i64_i32 v[74:75], s[16:17], v3, s21, v[162:163]
	v_lshl_add_u64 v[78:79], v[164:165], 0, s[0:1]
	v_lshl_add_u64 v[82:83], v[166:167], 0, s[0:1]
	global_load_dwordx4 v[66:69], v[66:67], off
	s_nop 0
	global_load_dwordx4 v[74:77], v[74:75], off
	s_nop 0
	global_load_dwordx4 v[78:81], v[78:79], off
	s_nop 0
	global_load_dwordx4 v[82:85], v[82:83], off
	s_cmp_lt_i32 s27, -4
	s_waitcnt vmcnt(3)
	ds_write_b128 v178, v[66:69]
	s_waitcnt vmcnt(2)
	ds_write_b128 v178, v[74:77] offset:8704
	s_waitcnt vmcnt(1)
	ds_write_b128 v180, v[78:81] offset:17408
	s_waitcnt vmcnt(0)
	ds_write_b128 v180, v[82:85] offset:26624
	s_waitcnt lgkmcnt(0)
	s_barrier
	s_cbranch_scc1 .LBB0_2771
	s_cmp_eq_u32 s98, 0
	s_cbranch_scc1 .Latt_lead0
	s_barrier
.Latt_lead0:
	v_and_b32_e32 v5, 64, v182
	v_xor_b32_e32 v3, 16, v182
	v_add_u32_e32 v5, 64, v5
	v_cmp_lt_i32_e32 vcc, v3, v5
	s_add_i32 s11, s27, 5
	s_sub_i32 s33, -5, s27
	v_cndmask_b32_e32 v3, v182, v3, vcc
	v_lshlrev_b32_e32 v185, 2, v3
	v_xor_b32_e32 v3, 32, v182
	v_cmp_lt_i32_e32 vcc, v3, v5
	s_max_i32 s34, s11, s33
	s_lshl_b32 s29, s14, 12
	v_cndmask_b32_e32 v3, v182, v3, vcc
	v_lshlrev_b32_e32 v186, 2, v3
	v_cvt_f32_u32_e32 v3, s34
	s_lshl_b32 s0, s13, 7
	s_bitset1_b32 s29, 9
	s_or_b32 s35, s0, s20
	v_rcp_iflag_f32_e32 v3, v3
	s_add_i32 s36, s29, s35
	v_or_b32_e32 v5, s36, v172
	v_mad_i64_i32 v[168:169], s[0:1], v5, s21, 0
	v_mul_f32_e32 v3, 0x4f7ffffe, v3
	v_cvt_u32_f32_e32 v3, v3
	v_or_b32_e32 v5, 16, v5
	v_mad_i64_i32 v[170:171], s[0:1], v5, s21, 0
	s_sub_i32 s0, 0, s34
	v_readfirstlane_b32 s1, v3
	s_mul_i32 s0, s0, s1
	s_lshl_b32 s31, s10, 2
	s_mul_hi_u32 s0, s1, s0
	s_sub_i32 s39, s2, s12
	s_lshl_b32 s6, s11, 1
	s_lshl_b32 s30, s14, 8
	s_mov_b32 s10, 0
	s_add_i32 s31, s31, s19
	s_ashr_i32 s37, s11, 31
	s_add_i32 s38, s1, s0
	s_add_i32 s39, s39, -4
	s_mov_b32 s41, 0
	s_mov_b32 s11, 0
	s_mov_b32 s42, 0

; __device__ __forceinline__ void phase_attention(const Frame& F, const Args& a) {
;     ...
;                 float mx = s[m][0][0];
; #pragma unroll
;                 for (int nn = 0; nn < 4; ++nn)
; #pragma unroll
;                     for (int j = 0; j < 4; ++j) mx = fmaxf(mx, s[m][nn][j]);
;                 mx = fmaxf(mx, __shfl_xor(mx, 16)); mx = fmaxf(mx, __shfl_xor(mx, 32));
;                 const float mnew = fmaxf(mrun[m], mx), alpha = __expf(mrun[m] - mnew); mrun[m] = mnew;
;                 float rs = 0.f;
; #pragma unroll
;                 for (int nn = 0; nn < 4; ++nn)
; #pragma unroll
;                     for (int j = 0; j < 4; ++j) { const float p = __expf(s[m][nn][j] - mnew); s[m][nn][j] = p; rs += p; }
;                 rs += __shfl_xor(rs, 16); rs += __shfl_xor(rs, 32);
;                 lrun[m] = lrun[m] * alpha + rs;
; #pragma unroll
;                 for (int nd = 0; nd < 8; ++nd) o[m][nd] = o[m][nd] * alpha;
;     ...
;             if (step + 1 < nstep) ATT_STORE((step + 1) & 1);
;             __syncthreads();
.LBB0_2786:
	s_cmp_eq_u32 s98, 0
	s_cbranch_scc1 .Latt_mid0
	s_andn2_b64 vcc, exec, s[14:15]
	s_cbranch_vccnz .Latt_mid0
	s_bitcmp1_b32 s40, 0
	s_cselect_b32 s99, 0x8c00, 0
	v_add3_u32 v224, s99, v177, v150
	ds_write_b128 v224, v[66:69]
	ds_write_b128 v224, v[74:77] offset:8704
	v_add3_u32 v224, s99, v179, v154
	ds_write_b128 v224, v[78:81] offset:17408
	ds_write_b128 v224, v[82:85] offset:26624
.Latt_mid0:
	s_waitcnt lgkmcnt(0)
	s_barrier
	s_waitcnt lgkmcnt(0)
	v_add_f32_e32 v5, v142, v143
	v_max_f32_e32 v142, v139, v139
	v_max_f32_e32 v143, v138, v138
	v_max_f32_e32 v142, v143, v142
	v_max3_f32 v142, v142, v140, v141
	v_max3_f32 v142, v142, v134, v135
	v_max3_f32 v142, v142, v136, v137
	v_max3_f32 v142, v142, v130, v131
	v_max3_f32 v142, v142, v132, v133
	v_max3_f32 v142, v142, v122, v123
	v_max3_f32 v142, v142, v124, v125
	ds_bpermute_b32 v143, v185, v142
	v_sub_f32_e32 v4, v4, v3
	v_mul_f32_e32 v4, 0x3fb8aa3b, v4
	v_exp_f32_e32 v4, v4
	s_add_i32 s0, s39, s42
	s_waitcnt lgkmcnt(0)
	v_max_f32_e32 v143, v143, v143
	v_max_f32_e32 v142, v142, v143
	ds_bpermute_b32 v143, v186, v142
	v_fmac_f32_e32 v5, v189, v4
	v_pk_mul_f32 v[116:117], v[116:117], v[4:5] op_sel_hi:[1,0]
	v_pk_mul_f32 v[114:115], v[114:115], v[4:5] op_sel_hi:[1,0]
	v_pk_mul_f32 v[112:113], v[112:113], v[4:5] op_sel_hi:[1,0]
	s_waitcnt lgkmcnt(0)
	v_max3_f32 v142, v187, v142, v143
	v_sub_f32_e32 v138, v138, v142
	v_mul_f32_e32 v138, 0x3fb8aa3b, v138
	v_sub_f32_e32 v139, v139, v142
	v_exp_f32_e32 v138, v138
	v_mul_f32_e32 v139, 0x3fb8aa3b, v139
	v_sub_f32_e32 v140, v140, v142
	v_exp_f32_e32 v139, v139
	v_mul_f32_e32 v140, 0x3fb8aa3b, v140
	v_sub_f32_e32 v141, v141, v142
	v_exp_f32_e32 v140, v140
	v_mul_f32_e32 v141, 0x3fb8aa3b, v141
	v_sub_f32_e32 v134, v134, v142
	v_exp_f32_e32 v141, v141
	v_mul_f32_e32 v134, 0x3fb8aa3b, v134
	v_sub_f32_e32 v135, v135, v142
	v_add_f32_e32 v143, 0, v138
	v_exp_f32_e32 v134, v134
	v_mul_f32_e32 v135, 0x3fb8aa3b, v135
	v_sub_f32_e32 v136, v136, v142
	v_sub_f32_e32 v130, v130, v142
	v_add_f32_e32 v143, v139, v143
	v_exp_f32_e32 v135, v135
	v_mul_f32_e32 v136, 0x3fb8aa3b, v136
	v_sub_f32_e32 v137, v137, v142
	v_mul_f32_e32 v130, 0x3fb8aa3b, v130
	v_add_f32_e32 v143, v140, v143
	v_exp_f32_e32 v136, v136
	v_mul_f32_e32 v137, 0x3fb8aa3b, v137
	v_exp_f32_e32 v144, v130
	v_sub_f32_e32 v130, v131, v142
	v_add_f32_e32 v143, v141, v143
	v_exp_f32_e32 v137, v137
	v_mul_f32_e32 v130, 0x3fb8aa3b, v130
	v_add_f32_e32 v143, v134, v143
	v_exp_f32_e32 v145, v130
	v_sub_f32_e32 v130, v132, v142
	v_add_f32_e32 v143, v135, v143
	v_mul_f32_e32 v130, 0x3fb8aa3b, v130
	v_add_f32_e32 v143, v136, v143
	v_exp_f32_e32 v146, v130
	v_sub_f32_e32 v130, v133, v142
	v_sub_f32_e32 v122, v122, v142
	v_add_f32_e32 v143, v137, v143
	v_mul_f32_e32 v130, 0x3fb8aa3b, v130
	v_mul_f32_e32 v122, 0x3fb8aa3b, v122
	v_exp_f32_e32 v147, v130
	v_add_f32_e32 v130, v144, v143
	v_exp_f32_e32 v143, v122
	v_sub_f32_e32 v122, v123, v142
	v_mul_f32_e32 v122, 0x3fb8aa3b, v122
	v_exp_f32_e32 v123, v122
	v_sub_f32_e32 v122, v124, v142
	v_mul_f32_e32 v122, 0x3fb8aa3b, v122
	v_add_f32_e32 v130, v145, v130
	v_exp_f32_e32 v124, v122
	v_sub_f32_e32 v122, v125, v142
	v_add_f32_e32 v130, v146, v130
	v_mul_f32_e32 v122, 0x3fb8aa3b, v122
	v_add_f32_e32 v130, v147, v130
	v_exp_f32_e32 v125, v122
	v_add_f32_e32 v122, v143, v130
	v_add_f32_e32 v122, v123, v122
	v_add_f32_e32 v122, v124, v122
	v_add_f32_e32 v122, v125, v122
	ds_bpermute_b32 v130, v185, v122
	v_pk_mul_f32 v[110:111], v[110:111], v[4:5] op_sel_hi:[1,0]
	v_pk_mul_f32 v[96:97], v[96:97], v[4:5] op_sel_hi:[1,0]
	v_pk_mul_f32 v[94:95], v[94:95], v[4:5] op_sel_hi:[1,0]
	v_pk_mul_f32 v[100:101], v[100:101], v[4:5] op_sel_hi:[1,0]
	s_waitcnt lgkmcnt(0)
	v_add_f32_e32 v122, v122, v130
	v_pk_mul_f32 v[98:99], v[98:99], v[4:5] op_sel_hi:[1,0]
	v_pk_mul_f32 v[104:105], v[104:105], v[4:5] op_sel_hi:[1,0]
	v_pk_mul_f32 v[102:103], v[102:103], v[4:5] op_sel_hi:[1,0]
	v_pk_mul_f32 v[108:109], v[108:109], v[4:5] op_sel_hi:[1,0]
	v_pk_mul_f32 v[106:107], v[106:107], v[4:5] op_sel_hi:[1,0]
	v_pk_mul_f32 v[88:89], v[88:89], v[4:5] op_sel_hi:[1,0]
	v_pk_mul_f32 v[86:87], v[86:87], v[4:5] op_sel_hi:[1,0]
	v_pk_mul_f32 v[92:93], v[92:93], v[4:5] op_sel_hi:[1,0]
	v_pk_mul_f32 v[90:91], v[90:91], v[4:5] op_sel_hi:[1,0]
	v_sub_f32_e32 v4, v187, v142
	ds_bpermute_b32 v130, v186, v122
	v_mul_f32_e32 v4, 0x3fb8aa3b, v4
	v_exp_f32_e32 v4, v4
	s_add_i32 s0, s0, s43
	s_waitcnt lgkmcnt(0)
; #define GAS __attribute__((address_space(1)))
; #define LAS __attribute__((address_space(3)))
; __device__ __forceinline__ unsigned pk4_fp8(float a, float b, float c, float d) { int w = 0; w = __builtin_amdgcn_cvt_pk_fp8_f32(sat8(a), sat8(b), w, false); w = __builtin_amdgcn_cvt_pk_fp8_f32(sat8(c), sat8(d), w, true); return (unsigned)w; }
; __device__ __forceinline__ unsigned cvt_pk_bf16(float lo, float hi) { unsigned r; asm volatile("v_cvt_pk_bf16_f32 %0, %1, %2" : "=v"(r) : "v"(lo), "v"(hi)); return r; }
; __device__ __forceinline__ void phase_attention(const Frame& F, const Args& a) {
;     ...
;                 rs += __shfl_xor(rs, 16); rs += __shfl_xor(rs, 32);
;                 lrun[m] = lrun[m] * alpha + rs;
; #pragma unroll
;                 for (int nd = 0; nd < 8; ++nd) o[m][nd] = o[m][nd] * alpha;
; #pragma unroll
;                 for (int ks = 0; ks < 2; ++ks) { u32x4 w; w.x = cvt_pk_bf16(s[m][2 * ks][0], s[m][2 * ks][1]); w.y = cvt_pk_bf16(s[m][2 * ks][2], s[m][2 * ks][3]);
;                     w.z = cvt_pk_bf16(s[m][2 * ks + 1][0], s[m][2 * ks + 1][1]); w.w = cvt_pk_bf16(s[m][2 * ks + 1][2], s[m][2 * ks + 1][3]); pf[m][ks] = __builtin_bit_cast(bf16x8, w); }
;             }
;             __builtin_amdgcn_s_setprio(1);
; #pragma unroll
;             for (int ks = 0; ks < 2; ++ks)
; #pragma unroll
;                 for (int nd = 0; nd < 8; ++nd) { const LAS bf16_t* vp = Vs + (16 * nd + fr) * 72 + 32 * ks + 4 * fq;
;                     u32x4 w; const u32x2 lo = *(const LAS u32x2*)vp, hi = *(const LAS u32x2*)(vp + 16); w.x = lo.x; w.y = lo.y; w.z = hi.x; w.w = hi.y;
;                     const bf16x8 vf = __builtin_bit_cast(bf16x8, w);
; #pragma unroll
;                     for (int m = 0; m < 2; ++m) o[m][nd] = __builtin_amdgcn_mfma_f32_16x16x32_bf16(vf, pf[m][ks], o[m][nd], 0, 0, 0); }
;             __builtin_amdgcn_s_setprio(0);
;             if (ti == ntile - 1) {
; #pragma unroll
;                 for (int m = 0; m < 2; ++m) { const float inv = 16.0f / lrun[m]; unsigned char* op = (unsigned char*)O + (size_t)(qrow + 16 * m + fr) * D + qh * 128 + 4 * fq;
; #pragma unroll
;                     for (int nd = 0; nd < 8; ++nd) { const f32x4 v = o[m][nd] * inv; *(GAS unsigned*)(op + 16 * nd) = pk4_fp8(v[0], v[1], v[2], v[3]); } }
;             }
;             if (step + 1 < nstep) ATT_STORE((step + 1) & 1);
	v_add_f32_e32 v122, v122, v130
	v_fmac_f32_e32 v122, v188, v4
	v_pk_mul_f32 v[72:73], v[72:73], v[4:5] op_sel_hi:[1,0]
	v_pk_mul_f32 v[70:71], v[70:71], v[4:5] op_sel_hi:[1,0]
	v_pk_mul_f32 v[64:65], v[64:65], v[4:5] op_sel_hi:[1,0]
	v_pk_mul_f32 v[62:63], v[62:63], v[4:5] op_sel_hi:[1,0]
	v_pk_mul_f32 v[60:61], v[60:61], v[4:5] op_sel_hi:[1,0]
	v_pk_mul_f32 v[58:59], v[58:59], v[4:5] op_sel_hi:[1,0]
	v_pk_mul_f32 v[56:57], v[56:57], v[4:5] op_sel_hi:[1,0]
	v_pk_mul_f32 v[54:55], v[54:55], v[4:5] op_sel_hi:[1,0]
	v_pk_mul_f32 v[52:53], v[52:53], v[4:5] op_sel_hi:[1,0]
	v_pk_mul_f32 v[50:51], v[50:51], v[4:5] op_sel_hi:[1,0]
	v_pk_mul_f32 v[48:49], v[48:49], v[4:5] op_sel_hi:[1,0]
	v_pk_mul_f32 v[46:47], v[46:47], v[4:5] op_sel_hi:[1,0]
	v_pk_mul_f32 v[44:45], v[44:45], v[4:5] op_sel_hi:[1,0]
	v_pk_mul_f32 v[42:43], v[42:43], v[4:5] op_sel_hi:[1,0]
	v_pk_mul_f32 v[40:41], v[40:41], v[4:5] op_sel_hi:[1,0]
	v_pk_mul_f32 v[38:39], v[38:39], v[4:5] op_sel_hi:[1,0]
	v_cvt_pk_bf16_f32 v130, v138, v139
	v_cvt_pk_bf16_f32 v131, v140, v141
	v_cvt_pk_bf16_f32 v132, v134, v135
	v_cvt_pk_bf16_f32 v133, v136, v137
	v_cvt_pk_bf16_f32 v134, v144, v145
	v_cvt_pk_bf16_f32 v135, v146, v147
	v_cvt_pk_bf16_f32 v136, v143, v123
	v_cvt_pk_bf16_f32 v137, v124, v125
	s_setprio 1
	v_add3_u32 v4, s44, v151, v176
	v_add_u32_e32 v123, 0x4000, v4
	ds_read2_b64 v[138:141], v123 offset0:128 offset1:132
	v_add_u32_e32 v143, 0x4800, v4
	v_add_u32_e32 v144, 0x5000, v4
	v_add_u32_e32 v145, 0x5800, v4
	v_add_u32_e32 v146, 0x6800, v4
	v_add_u32_e32 v147, 0x7000, v4
	v_add_u32_e32 v148, 0x7800, v4
	v_add_u32_e32 v4, 0x8000, v4
	s_waitcnt lgkmcnt(0)
	v_mfma_f32_16x16x32_bf16 v[114:117], v[138:141], v[126:129], v[114:117]
	v_mfma_f32_16x16x32_bf16 v[70:73], v[138:141], v[130:133], v[70:73]
	ds_read2_b64 v[138:141], v143 offset0:160 offset1:164
	s_waitcnt lgkmcnt(0)
	v_mfma_f32_16x16x32_bf16 v[110:113], v[138:141], v[126:129], v[110:113]
	v_mfma_f32_16x16x32_bf16 v[62:65], v[138:141], v[130:133], v[62:65]
	ds_read2_b64 v[138:141], v144 offset0:192 offset1:196
	s_waitcnt lgkmcnt(0)
	v_mfma_f32_16x16x32_bf16 v[94:97], v[138:141], v[126:129], v[94:97]
	v_mfma_f32_16x16x32_bf16 v[58:61], v[138:141], v[130:133], v[58:61]
	ds_read2_b64 v[138:141], v145 offset0:224 offset1:228
	s_waitcnt lgkmcnt(0)
	v_mfma_f32_16x16x32_bf16 v[98:101], v[138:141], v[126:129], v[98:101]
	v_mfma_f32_16x16x32_bf16 v[54:57], v[138:141], v[130:133], v[54:57]
	ds_read2_b64 v[138:141], v146 offset1:4
	s_waitcnt lgkmcnt(0)
	v_mfma_f32_16x16x32_bf16 v[102:105], v[138:141], v[126:129], v[102:105]
	v_mfma_f32_16x16x32_bf16 v[50:53], v[138:141], v[130:133], v[50:53]
	ds_read2_b64 v[138:141], v147 offset0:32 offset1:36
	s_waitcnt lgkmcnt(0)
	v_mfma_f32_16x16x32_bf16 v[106:109], v[138:141], v[126:129], v[106:109]
	v_mfma_f32_16x16x32_bf16 v[46:49], v[138:141], v[130:133], v[46:49]
	ds_read2_b64 v[138:141], v148 offset0:64 offset1:68
	s_waitcnt lgkmcnt(0)
	v_mfma_f32_16x16x32_bf16 v[86:89], v[138:141], v[126:129], v[86:89]
	v_mfma_f32_16x16x32_bf16 v[42:45], v[138:141], v[130:133], v[42:45]
	ds_read2_b64 v[138:141], v4 offset0:96 offset1:100
	s_waitcnt lgkmcnt(0)
	v_mfma_f32_16x16x32_bf16 v[90:93], v[138:141], v[126:129], v[90:93]
	ds_read2_b64 v[124:127], v123 offset0:136 offset1:140
	s_waitcnt lgkmcnt(0)
	v_mfma_f32_16x16x32_bf16 v[114:117], v[124:127], v[118:121], v[114:117]
	v_mfma_f32_16x16x32_bf16 v[70:73], v[124:127], v[134:137], v[70:73]
	ds_read2_b64 v[124:127], v143 offset0:168 offset1:172
	s_waitcnt lgkmcnt(0)
	v_mfma_f32_16x16x32_bf16 v[110:113], v[124:127], v[118:121], v[110:113]
	v_mfma_f32_16x16x32_bf16 v[62:65], v[124:127], v[134:137], v[62:65]
	ds_read2_b64 v[124:127], v144 offset0:200 offset1:204
	s_waitcnt lgkmcnt(0)
	v_mfma_f32_16x16x32_bf16 v[94:97], v[124:127], v[118:121], v[94:97]
	v_mfma_f32_16x16x32_bf16 v[58:61], v[124:127], v[134:137], v[58:61]
	ds_read2_b64 v[124:127], v145 offset0:232 offset1:236
	s_waitcnt lgkmcnt(0)
	v_mfma_f32_16x16x32_bf16 v[98:101], v[124:127], v[118:121], v[98:101]
	v_mfma_f32_16x16x32_bf16 v[54:57], v[124:127], v[134:137], v[54:57]
	ds_read2_b64 v[124:127], v146 offset0:8 offset1:12
	s_waitcnt lgkmcnt(0)
	v_mfma_f32_16x16x32_bf16 v[102:105], v[124:127], v[118:121], v[102:105]
	v_mfma_f32_16x16x32_bf16 v[50:53], v[124:127], v[134:137], v[50:53]
	ds_read2_b64 v[124:127], v147 offset0:40 offset1:44
	s_waitcnt lgkmcnt(0)
	v_mfma_f32_16x16x32_bf16 v[106:109], v[124:127], v[118:121], v[106:109]
	v_mfma_f32_16x16x32_bf16 v[46:49], v[124:127], v[134:137], v[46:49]
	ds_read2_b64 v[124:127], v148 offset0:72 offset1:76
	s_waitcnt lgkmcnt(0)
	v_mfma_f32_16x16x32_bf16 v[86:89], v[124:127], v[118:121], v[86:89]
	v_mfma_f32_16x16x32_bf16 v[42:45], v[124:127], v[134:137], v[42:45]
	ds_read2_b64 v[124:127], v4 offset0:104 offset1:108
	v_mfma_f32_16x16x32_bf16 v[38:41], v[138:141], v[130:133], v[38:41]
	s_waitcnt lgkmcnt(0)
	v_mfma_f32_16x16x32_bf16 v[90:93], v[124:127], v[118:121], v[90:93]
	v_mfma_f32_16x16x32_bf16 v[38:41], v[124:127], v[134:137], v[38:41]
	s_setprio 0
	s_cmp_lg_u32 s0, 0
	s_cbranch_scc0 .LBB0_2791
	s_andn2_b64 vcc, exec, s[14:15]
	s_cbranch_vccnz .LBB0_2789
.LBB0_2788:
	s_cmp_lg_u32 s98, 0
	s_cbranch_scc1 .LBB0_2789
	s_bitcmp1_b32 s40, 0
	s_cselect_b32 s0, 0x8c00, 0
	s_add_i32 s0, s0, 0
	v_add3_u32 v4, s0, v177, v150
	ds_write_b128 v4, v[66:69]
	ds_write_b128 v4, v[74:77] offset:8704
	v_add3_u32 v4, s0, v179, v154
	ds_write_b128 v4, v[78:81] offset:17408
	ds_write_b128 v4, v[82:85] offset:26624
